# P8 near-empty blocks scheduled after each group's full blocks (full rounds stay in lockstep)
# baseline (speedup 1.0000x reference)
; #define LAS __attribute__((address_space(3)))
;     __device__ __forceinline__ bool next(int i, pg8::Unit& u) const {
;         const int NB = __builtin_amdgcn_readfirstlane(tab[0]); const int L = i * G + c; if (L >= NB * nN) return false;
;         const int b = L / nN, pn = L - b * nN, e = __builtin_amdgcn_readfirstlane(tab[64 + b]);
;         u.pa = A; u.pb = B + (size_t)e * bexp + (size_t)pn * 256 * 128; u.row0 = b * 256; u.col0 = pn * 256; u.aux = e; u.blk = b; return true;
;     }
; __device__ __forceinline__ void moe_tables(Ctx& X) {
;     LAS int* tab = (LAS int*)(X.lds + LDS_TAB);
;     if (X.tid < 64) { const int e = X.tid;
;         const int cnt = (e < NE) ? (int)__hip_atomic_load(XP_ctl(X) + CW_CNT + 64 * e, __ATOMIC_RELAXED, __HIP_MEMORY_SCOPE_AGENT) : 0; const int k = (cnt + 255) >> 8;
;         int incl = k;
; #pragma unroll
;         for (int o = 1; o < 64; o <<= 1) { const int t = __shfl_up(incl, o); if (e >= o) incl += t; }
;         const int first = incl - k;
;         if (e < NE) { tab[8 + e] = first; for (int b = 0; b < k; ++b) { if (first + b < MAXBLK) { tab[64 + first + b] = e; tab[256 + first + b] = (cnt - 256 * b) < 256 ? (cnt - 256 * b) : 256; } } }
;         if (e == NE - 1) { tab[8 + NE] = incl; tab[0] = incl < MAXBLK ? incl : MAXBLK; } }
;     __syncthreads();
.LBB0_917:
	s_or_b64 exec, exec, s[8:9]
	s_waitcnt lgkmcnt(0)
	s_barrier
	s_cmp_lg_u32 s93, 0
	s_cbranch_scc1 .Lsch7_done
	s_and_b32 s99, s87, 7
	s_lshr_b32 s101, s87, 3
	s_and_b32 s98, s99, 3
	s_lshl_b32 s98, s98, 2
	s_lshr_b32 s100, s101, 3
	s_or_b32 s98, s98, s100
	s_lshr_b32 s99, s99, 2
	s_lshl_b32 s99, s99, 3
	s_and_b32 s101, s101, 7
	s_or_b32 s101, s101, s99
	s_lshr_b32 s99, s98, 2
	s_and_b32 s100, s98, 3
	s_lshl_b32 s100, s100, 2
	s_or_b32 s99, s99, s100
	v_and_b32_e32 v2, 63, v0
	v_lshlrev_b32_e32 v3, 2, v2
	v_add_u32_e32 v3, 0x23c00, v3
	v_mov_b32_e32 v4, 0x7fff0000
	ds_write_b32 v3, v4
	v_min_u32_e32 v5, 31, v2
	v_lshlrev_b32_e32 v5, 2, v5
	v_add_u32_e32 v5, 0x22020, v5
	ds_read2_b32 v[6:7], v5 offset1:1
	s_waitcnt lgkmcnt(0)
	v_sub_u32_e32 v8, v7, v6
	v_add_u32_e32 v9, -1, v7
	v_max_i32_e32 v9, 0, v9
	v_lshlrev_b32_e32 v9, 2, v9
	v_add_u32_e32 v9, 0x22400, v9
	ds_read_b32 v9, v9
	s_waitcnt lgkmcnt(0)
	v_cmp_gt_i32_e32 vcc, 0x81, v9
	v_cmp_lt_i32_e64 s[10:11], 0, v8
	s_and_b64 vcc, vcc, s[10:11]
	v_cmp_gt_u32_e64 s[10:11], 32, v2
	s_and_b64 vcc, vcc, s[10:11]
	v_cndmask_b32_e64 v10, 0, 1, vcc
	v_cndmask_b32_e64 v8, 0, v8, s[10:11]
	v_sub_u32_e32 v11, v8, v10
	v_lshl_or_b32 v13, v10, 16, v11
	s_nop 1
	v_add_u32_dpp v13, v13, v13 row_shr:1 row_mask:0xf bank_mask:0xf bound_ctrl:0
	s_nop 1
	v_add_u32_dpp v13, v13, v13 row_shr:2 row_mask:0xf bank_mask:0xf bound_ctrl:0
	s_nop 1
	v_add_u32_dpp v13, v13, v13 row_shr:4 row_mask:0xf bank_mask:0xf bound_ctrl:0
	s_nop 1
	v_add_u32_dpp v13, v13, v13 row_shr:8 row_mask:0xf bank_mask:0xf bound_ctrl:0
	s_nop 1
	v_add_u32_dpp v13, v13, v13 row_bcast:15 row_mask:0xa bank_mask:0xf
	s_nop 1
	v_and_b32_e32 v14, 0xffff, v13
	v_sub_u32_e32 v14, v14, v11
	v_lshrrev_b32_e32 v15, 16, v13
	v_sub_u32_e32 v15, v15, v10
	v_add_u32_e32 v16, v14, v11
	v_add_u32_e32 v17, -1, v8
	v_mov_b32_e32 v18, v15
	s_mov_b32 s12, 0
	s_mov_b64 s[8:9], exec
.Lsch7_loop:
	s_mov_b64 exec, s[8:9]
	v_cmp_lt_i32_e32 vcc, s12, v8
	s_and_b64 exec, exec, vcc
	s_cbranch_execz .Lsch7_end
	v_cmp_eq_u32_e32 vcc, s12, v17
	v_cmp_eq_u32_e64 s[10:11], 1, v10
	s_and_b64 vcc, vcc, s[10:11]
	v_add_u32_e32 v3, s12, v14
	v_cndmask_b32_e32 v4, v3, v15, vcc
	v_cndmask_b32_e32 v5, v18, v16, vcc
	v_mov_b32_e32 v7, s98
	v_mov_b32_e32 v9, s99
	v_cndmask_b32_e32 v12, v7, v9, vcc
	v_cndmask_b32_e32 v7, v9, v7, vcc
	v_and_b32_e32 v9, 15, v4
	v_cmp_eq_u32_e32 vcc, v9, v12
	v_lshrrev_b32_e32 v4, 4, v4
	v_add_u32_e32 v5, 15, v5
	v_sub_u32_e32 v5, v5, v7
	v_lshrrev_b32_e32 v5, 4, v5
	v_add_u32_e32 v4, v4, v5
	v_lshlrev_b32_e32 v4, 2, v4
	v_add_u32_e32 v4, 0x23c00, v4
	v_add_u32_e32 v5, s12, v6
	v_lshl_or_b32 v5, v5, 4, s101
	s_and_b64 exec, exec, vcc
	ds_write_b32 v4, v5
	s_add_i32 s12, s12, 1
	s_branch .Lsch7_loop

; #define LAS __attribute__((address_space(3)))
;     __device__ __forceinline__ bool next(int i, pg8::Unit& u) const {
;         const int NB = __builtin_amdgcn_readfirstlane(tab[0]); const int L = i * G + c; if (L >= NB * nN) return false;
;         const int b = L / nN, pn = L - b * nN, e = __builtin_amdgcn_readfirstlane(tab[64 + b]);
;         u.pa = A; u.pb = B + (size_t)e * bexp + (size_t)pn * 256 * 128; u.row0 = b * 256; u.col0 = pn * 256; u.aux = e; u.blk = b; return true;
;     }
; __device__ __forceinline__ void moe_tables(Ctx& X) {
;     LAS int* tab = (LAS int*)(X.lds + LDS_TAB);
;     if (X.tid < 64) { const int e = X.tid;
;         const int cnt = (e < NE) ? (int)__hip_atomic_load(XP_ctl(X) + CW_CNT + 64 * e, __ATOMIC_RELAXED, __HIP_MEMORY_SCOPE_AGENT) : 0; const int k = (cnt + 255) >> 8;
;         int incl = k;
; #pragma unroll
;         for (int o = 1; o < 64; o <<= 1) { const int t = __shfl_up(incl, o); if (e >= o) incl += t; }
;         const int first = incl - k;
;         if (e < NE) { tab[8 + e] = first; for (int b = 0; b < k; ++b) { if (first + b < MAXBLK) { tab[64 + first + b] = e; tab[256 + first + b] = (cnt - 256 * b) < 256 ? (cnt - 256 * b) : 256; } } }
;         if (e == NE - 1) { tab[8 + NE] = incl; tab[0] = incl < MAXBLK ? incl : MAXBLK; } }
;     __syncthreads();
.LBB0_1022:
	s_cmp_lg_u32 s93, 0
	s_cbranch_scc1 .Lsch8_done
	s_and_b32 s98, s87, 7
	s_lshl_b32 s98, s98, 2
	s_lshr_b32 s100, s87, 6
	s_or_b32 s98, s98, s100
	s_bfe_u32 s101, s87, 0x30003
	s_lshr_b32 s99, s98, 2
	s_and_b32 s100, s98, 3
	s_lshl_b32 s100, s100, 3
	s_or_b32 s99, s99, s100
	v_and_b32_e32 v2, 63, v0
	v_lshlrev_b32_e32 v3, 2, v2
	v_add_u32_e32 v3, 0x23c00, v3
	v_mov_b32_e32 v4, 0x7fff0000
	ds_write_b32 v3, v4
	v_min_u32_e32 v5, 31, v2
	v_lshlrev_b32_e32 v5, 2, v5
	v_add_u32_e32 v5, 0x22020, v5
	ds_read2_b32 v[6:7], v5 offset1:1
	s_waitcnt lgkmcnt(0)
	v_sub_u32_e32 v8, v7, v6
	v_add_u32_e32 v9, -1, v7
	v_max_i32_e32 v9, 0, v9
	v_lshlrev_b32_e32 v9, 2, v9
	v_add_u32_e32 v9, 0x22400, v9
	ds_read_b32 v9, v9
	s_waitcnt lgkmcnt(0)
	v_cmp_gt_i32_e32 vcc, 0x81, v9
	v_cmp_lt_i32_e64 s[10:11], 0, v8
	s_and_b64 vcc, vcc, s[10:11]
	v_cmp_gt_u32_e64 s[10:11], 32, v2
	s_and_b64 vcc, vcc, s[10:11]
	v_cndmask_b32_e64 v10, 0, 1, vcc
	v_cndmask_b32_e64 v8, 0, v8, s[10:11]
	v_sub_u32_e32 v11, v8, v10
	v_lshl_or_b32 v13, v10, 16, v11
	s_nop 1
	v_add_u32_dpp v13, v13, v13 row_shr:1 row_mask:0xf bank_mask:0xf bound_ctrl:0
	s_nop 1
	v_add_u32_dpp v13, v13, v13 row_shr:2 row_mask:0xf bank_mask:0xf bound_ctrl:0
	s_nop 1
	v_add_u32_dpp v13, v13, v13 row_shr:4 row_mask:0xf bank_mask:0xf bound_ctrl:0
	s_nop 1
	v_add_u32_dpp v13, v13, v13 row_shr:8 row_mask:0xf bank_mask:0xf bound_ctrl:0
	s_nop 1
	v_add_u32_dpp v13, v13, v13 row_bcast:15 row_mask:0xa bank_mask:0xf
	s_nop 1
	v_and_b32_e32 v14, 0xffff, v13
	v_sub_u32_e32 v14, v14, v11
	v_lshrrev_b32_e32 v15, 16, v13
	v_sub_u32_e32 v15, v15, v10
	v_add_u32_e32 v16, v14, v11
	v_add_u32_e32 v17, -1, v8
	v_readlane_b32 s12, v13, 31
	s_and_b32 s12, s12, 0xffff
	v_mov_b32_e32 v16, s12
	v_mov_b32_e32 v18, 0
	s_mov_b32 s12, 0
	s_mov_b64 s[8:9], exec
.Lsch8_loop:
	s_mov_b64 exec, s[8:9]
	v_cmp_lt_i32_e32 vcc, s12, v8
	s_and_b64 exec, exec, vcc
	s_cbranch_execz .Lsch8_end
	v_cmp_eq_u32_e32 vcc, s12, v17
	v_cmp_eq_u32_e64 s[10:11], 1, v10
	s_and_b64 vcc, vcc, s[10:11]
	v_add_u32_e32 v3, s12, v14
	v_cndmask_b32_e32 v4, v3, v15, vcc
	v_cndmask_b32_e32 v5, v18, v16, vcc
	v_mov_b32_e32 v7, s98
	v_mov_b32_e32 v9, s99
	v_cndmask_b32_e32 v12, v7, v9, vcc
	v_cndmask_b32_e32 v7, v9, v7, vcc
	v_and_b32_e32 v9, 31, v4
	v_cmp_eq_u32_e32 vcc, v9, v12
	v_lshrrev_b32_e32 v4, 5, v4
	v_add_u32_e32 v5, 31, v5
	v_sub_u32_e32 v5, v5, v7
	v_lshrrev_b32_e32 v5, 5, v5
	v_add_u32_e32 v4, v4, v5
	v_lshlrev_b32_e32 v4, 2, v4
	v_add_u32_e32 v4, 0x23c00, v4
	v_add_u32_e32 v5, s12, v6
	v_lshl_or_b32 v5, v5, 3, s101
	s_and_b64 exec, exec, vcc
	ds_write_b32 v4, v5
	s_add_i32 s12, s12, 1
	s_branch .Lsch8_loop
